# v18: v16 + final-norm gain loads hoisted under the row-sum reduction (ph13) + norm1 gain/shift/scale vectors of 5 of 8 column groups loaded with the row data (ph2)
# speedup vs baseline: 1.0106x; 1.0087x over previous
; __device__ __forceinline__ unsigned pack_fp8x4(float a, float b, float c, float d) { int w = __builtin_amdgcn_cvt_pk_fp8_f32(a, b, 0, false); w = __builtin_amdgcn_cvt_pk_fp8_f32(c, d, w, true); return (unsigned)w; }
; __device__ __forceinline__ unsigned pk2(float lo, float hi) { const f32x2_t v = {lo, hi}; return __builtin_bit_cast(unsigned, __builtin_convertvector(v, bf16x2_hw)); }
; __device__ __forceinline__ void ph2_norm1(const Frame& F, const Args& A) {
;     ...
;     for (int row = gw; row < S_; row += 2 * NGW) {
;         const int rowb = row + NGW < S_ ? row + NGW : row;
;         const f32x4* xa = (const f32x4*)(x + (size_t)row * DM) + F.lane; const f32x4* xb = (const f32x4*)(x + (size_t)rowb * DM) + F.lane;
;         f32x4 va[8], vb[8]; float sa = 0.f, sb = 0.f;
; #pragma unroll
;         for (int j = 0; j < 8; ++j) { va[j] = xa[64 * j]; vb[j] = xb[64 * j]; }
; #pragma unroll
;         for (int j = 0; j < 8; ++j) { sa += (va[j].x * va[j].x + va[j].y * va[j].y) + (va[j].z * va[j].z + va[j].w * va[j].w); sb += (vb[j].x * vb[j].x + vb[j].y * vb[j].y) + (vb[j].z * vb[j].z + vb[j].w * vb[j].w); }
;         const float ra = 1.f / sqrtf(wave_sum(sa) * (1.f / DM) + EPS_), rb = 1.f / sqrtf(wave_sum(sb) * (1.f / DM) + EPS_);
;         unsigned long long* oa = (unsigned long long*)(XN + (size_t)row * DM) + F.lane; unsigned long long* ob = (unsigned long long*)(XN + (size_t)rowb * DM) + F.lane;
; #pragma unroll
;         for (int j = 0; j < 8; ++j) { const int col = 4 * F.lane + 256 * j;
;             const f32x4 g = *(const f32x4*)(g1 + col), sh = *(const f32x4*)(MOD + col), sc = *(const f32x4*)(MOD + 2048 + col);
;             const f32x4 ha = va[j] * ra * g * (sc + 1.f) + sh, hb = vb[j] * rb * g * (sc + 1.f) + sh;
;             oa[64 * j] = (unsigned long long)pk2(ha.x, ha.y) | ((unsigned long long)pk2(ha.z, ha.w) << 32);
;             ob[64 * j] = (unsigned long long)pk2(hb.x, hb.y) | ((unsigned long long)pk2(hb.z, hb.w) << 32);
;             ((unsigned*)((unsigned char*)(A.ws + WS_XN8) + (size_t)row * DM) + F.lane)[64 * j] = pg8::pack_fp8x4(ha.x, ha.y, ha.z, ha.w);
;             ((unsigned*)((unsigned char*)(A.ws + WS_XN8) + (size_t)rowb * DM) + F.lane)[64 * j] = pg8::pack_fp8x4(hb.x, hb.y, hb.z, hb.w); }
;     }
.LBB0_167:
	s_add_i32 s0, s16, s6
	s_cmpk_lt_i32 s0, 0x2000
	s_cselect_b32 s0, s0, s6
	global_load_dwordx4 v[30:33], v[114:115], off offset:-4096
	global_load_dwordx4 v[22:25], v[114:115], off offset:-3072
	global_load_dwordx4 v[26:29], v[114:115], off offset:-2048
	global_load_dwordx4 v[10:13], v[114:115], off offset:1024
	global_load_dwordx4 v[14:17], v[114:115], off
	global_load_dwordx4 v[18:21], v[114:115], off offset:-1024
	global_load_dwordx4 v[2:5], v[114:115], off offset:3072
	global_load_dwordx4 v[6:9], v[114:115], off offset:2048
	global_load_dwordx4 v[136:139], v[74:75], off
	v_lshl_add_u64 v[34:35], s[88:89], 0, v[118:119]
	s_ashr_i32 s1, s0, 31
	v_add_co_u32_e32 v120, vcc, s9, v34
	s_lshl_b64 s[2:3], s[0:1], 13
	s_nop 0
	v_addc_co_u32_e32 v121, vcc, 0, v35, vcc
	v_lshl_add_u64 v[34:35], v[66:67], 0, s[2:3]
	global_load_dwordx4 v[46:49], v[70:71], off
	global_load_dwordx4 v[50:53], v[72:73], off
	v_lshl_add_u64 v[36:37], s[88:89], 0, v[116:117]
	global_load_dwordx4 v[62:65], v[34:35], off offset:2048
	global_load_dwordx4 v[140:143], v[34:35], off
	global_load_dwordx4 v[144:147], v[34:35], off offset:1024
	global_load_dwordx4 v[58:61], v[34:35], off offset:3072
	v_add_co_u32_e32 v122, vcc, s18, v36
	v_mov_b32_e32 v175, 0
	s_nop 0
	v_addc_co_u32_e32 v123, vcc, 0, v37, vcc
	v_add_co_u32_e32 v34, vcc, s17, v34
	s_lshl_b64 s[20:21], s[0:1], 12
	s_nop 0
	v_addc_co_u32_e32 v35, vcc, 0, v35, vcc
	global_load_dwordx4 v[42:45], v[34:35], off offset:1024
	global_load_dwordx4 v[54:57], v[34:35], off
	global_load_dwordx4 v[38:41], v[34:35], off offset:2048
	s_nop 0
	global_load_dwordx4 v[34:37], v[34:35], off offset:3072
	global_load_dwordx4 v[188:191], v[70:71], off offset:1024
	global_load_dwordx4 v[192:195], v[80:81], off
	global_load_dwordx4 v[196:199], v[78:79], off
	global_load_dwordx4 v[200:203], v[70:71], off offset:2048
	global_load_dwordx4 v[204:207], v[84:85], off
	global_load_dwordx4 v[208:211], v[82:83], off
	global_load_dwordx4 v[212:215], v[70:71], off offset:3072
	global_load_dwordx4 v[216:219], v[88:89], off
	global_load_dwordx4 v[220:223], v[86:87], off
	global_load_dwordx4 v[224:227], v[90:91], off
	global_load_dwordx4 v[228:231], v[94:95], off
	global_load_dwordx4 v[232:235], v[92:93], off
	global_load_dwordx4 v[236:239], v[96:97], off
	global_load_dwordx4 v[240:243], v[100:101], off
	global_load_dwordx4 v[244:247], v[98:99], off
	s_lshl_b64 s[0:1], s[0:1], 11
	v_lshl_add_u64 v[124:125], v[76:77], 0, s[0:1]
	v_mov_b32_e32 v176, 0
	v_lshl_add_u64 v[126:127], v[68:69], 0, s[20:21]
	v_mov_b32_e32 v177, 0
	v_mov_b32_e32 v178, 0
	v_mov_b32_e32 v179, 0
	v_mov_b32_e32 v180, 0
	s_add_i32 s6, s6, s8
	v_lshl_add_u64 v[114:115], v[114:115], 0, s[10:11]
	v_lshl_add_u64 v[116:117], v[116:117], 0, s[12:13]
	v_lshl_add_u64 v[118:119], v[118:119], 0, s[14:15]
	s_cmpk_lt_i32 s6, 0x2000
	s_waitcnt vmcnt(33)
	v_mov_b32_e32 v150, v31
	s_waitcnt vmcnt(32)
	v_mov_b32_e32 v151, v23
	s_waitcnt vmcnt(31)
	v_pk_mul_f32 v[152:153], v[28:29], v[28:29]
	v_pk_mul_f32 v[154:155], v[26:27], v[26:27]
	s_waitcnt vmcnt(30)
	v_pk_mul_f32 v[156:157], v[12:13], v[12:13]
	v_pk_mul_f32 v[158:159], v[10:11], v[10:11]
	v_mov_b32_e32 v162, v33
	v_mov_b32_e32 v163, v25
	v_mov_b32_e32 v148, v30
	v_mov_b32_e32 v149, v22
	v_mov_b32_e32 v160, v32
	v_mov_b32_e32 v161, v24
	v_pk_mov_b32 v[170:171], v[154:155], v[152:153] op_sel:[1,0]
	v_mov_b32_e32 v155, v153
	v_pk_mov_b32 v[152:153], v[158:159], v[156:157] op_sel:[1,0]
	v_mov_b32_e32 v159, v157
	v_pk_mul_f32 v[150:151], v[150:151], v[150:151]
	v_pk_mul_f32 v[156:157], v[162:163], v[162:163]
	v_pk_fma_f32 v[148:149], v[148:149], v[148:149], v[150:151]
	v_pk_fma_f32 v[150:151], v[160:161], v[160:161], v[156:157]
	s_waitcnt vmcnt(28)
	v_mul_f32_e32 v128, v19, v19
	v_mul_f32_e32 v164, v21, v21
	s_waitcnt vmcnt(26)
	v_mul_f32_e32 v166, v7, v7
	v_mul_f32_e32 v168, v9, v9
	v_pk_add_f32 v[154:155], v[170:171], v[154:155]
	v_pk_add_f32 v[148:149], v[148:149], v[150:151]
	v_mul_f32_e32 v172, v14, v14
	v_mul_f32_e32 v173, v16, v16
	v_mul_f32_e32 v174, v17, v17
	v_mul_f32_e32 v181, v4, v4
	v_mul_f32_e32 v182, v5, v5
	v_mul_f32_e32 v183, v15, v15
	v_pk_fma_f32 v[162:163], v[18:19], v[18:19], v[128:129] op_sel_hi:[1,1,0]
	v_pk_fma_f32 v[164:165], v[20:21], v[20:21], v[164:165] op_sel_hi:[1,1,0]
	v_pk_fma_f32 v[166:167], v[6:7], v[6:7], v[166:167] op_sel_hi:[1,1,0]
	v_pk_fma_f32 v[168:169], v[8:9], v[8:9], v[168:169] op_sel_hi:[1,1,0]
	v_pk_add_f32 v[154:155], v[154:155], v[154:155] op_sel:[0,1] op_sel_hi:[1,0]
	v_pk_add_f32 v[148:149], v[148:149], v[148:149] op_sel:[0,1] op_sel_hi:[1,0]
	v_mov_b32_e32 v163, v173
	v_mov_b32_e32 v165, v174
	v_mov_b32_e32 v167, v181
	v_mov_b32_e32 v169, v182
	v_mov_b32_e32 v155, v183
	v_mov_b32_e32 v149, v172
	v_pk_add_f32 v[152:153], v[152:153], v[158:159]
	v_pk_add_f32 v[150:151], v[162:163], v[164:165]
	v_pk_add_f32 v[156:157], v[166:167], v[168:169]
	s_waitcnt vmcnt(22)
	v_pk_mul_f32 v[158:159], v[64:65], v[64:65]
	v_pk_mul_f32 v[160:161], v[62:63], v[62:63]
	v_pk_add_f32 v[148:149], v[148:149], v[154:155]
	s_waitcnt vmcnt(21)
	v_mov_b32_e32 v162, v141
	s_waitcnt vmcnt(20)
	v_mov_b32_e32 v163, v145
	v_mov_b32_e32 v166, v143
	v_mov_b32_e32 v167, v147
	v_mov_b32_e32 v154, v140
	v_mov_b32_e32 v155, v144
	v_mov_b32_e32 v164, v142
	v_mov_b32_e32 v165, v146
	v_pk_mov_b32 v[170:171], v[160:161], v[158:159] op_sel:[1,0]
	v_mov_b32_e32 v161, v159
	v_pk_add_f32 v[148:149], v[148:149], v[150:151]
	v_pk_mul_f32 v[150:151], v[162:163], v[162:163]
	v_pk_mul_f32 v[158:159], v[166:167], v[166:167]
	v_mul_f32_e32 v184, v3, v3
	v_mul_f32_e32 v185, v2, v2
	v_pk_add_f32 v[152:153], v[152:153], v[152:153] op_sel:[0,1] op_sel_hi:[1,0]
	v_pk_fma_f32 v[150:151], v[154:155], v[154:155], v[150:151]
	v_pk_fma_f32 v[154:155], v[164:165], v[164:165], v[158:159]
	v_pk_add_f32 v[148:149], v[148:149], v[148:149] op_sel:[0,1] op_sel_hi:[1,0]
	v_mov_b32_e32 v153, v184
	s_waitcnt vmcnt(19)
; __device__ __forceinline__ unsigned pack_fp8x4(float a, float b, float c, float d) { int w = __builtin_amdgcn_cvt_pk_fp8_f32(a, b, 0, false); w = __builtin_amdgcn_cvt_pk_fp8_f32(c, d, w, true); return (unsigned)w; }
; __device__ __forceinline__ unsigned pk2(float lo, float hi) { const f32x2_t v = {lo, hi}; return __builtin_bit_cast(unsigned, __builtin_convertvector(v, bf16x2_hw)); }
; __device__ __forceinline__ void ph2_norm1(const Frame& F, const Args& A) {
;     ...
;         for (int j = 0; j < 8; ++j) { sa += (va[j].x * va[j].x + va[j].y * va[j].y) + (va[j].z * va[j].z + va[j].w * va[j].w); sb += (vb[j].x * vb[j].x + vb[j].y * vb[j].y) + (vb[j].z * vb[j].z + vb[j].w * vb[j].w); }
;         const float ra = 1.f / sqrtf(wave_sum(sa) * (1.f / DM) + EPS_), rb = 1.f / sqrtf(wave_sum(sb) * (1.f / DM) + EPS_);
;         unsigned long long* oa = (unsigned long long*)(XN + (size_t)row * DM) + F.lane; unsigned long long* ob = (unsigned long long*)(XN + (size_t)rowb * DM) + F.lane;
; #pragma unroll
;         for (int j = 0; j < 8; ++j) { const int col = 4 * F.lane + 256 * j;
;             const f32x4 g = *(const f32x4*)(g1 + col), sh = *(const f32x4*)(MOD + col), sc = *(const f32x4*)(MOD + 2048 + col);
;             const f32x4 ha = va[j] * ra * g * (sc + 1.f) + sh, hb = vb[j] * rb * g * (sc + 1.f) + sh;
;             oa[64 * j] = (unsigned long long)pk2(ha.x, ha.y) | ((unsigned long long)pk2(ha.z, ha.w) << 32);
;             ob[64 * j] = (unsigned long long)pk2(hb.x, hb.y) | ((unsigned long long)pk2(hb.z, hb.w) << 32);
;             ((unsigned*)((unsigned char*)(A.ws + WS_XN8) + (size_t)row * DM) + F.lane)[64 * j] = pg8::pack_fp8x4(ha.x, ha.y, ha.z, ha.w);
;             ((unsigned*)((unsigned char*)(A.ws + WS_XN8) + (size_t)rowb * DM) + F.lane)[64 * j] = pg8::pack_fp8x4(hb.x, hb.y, hb.z, hb.w); }
	v_mul_f32_e32 v128, v59, v59
	v_mul_f32_e32 v168, v61, v61
	v_pk_add_f32 v[158:159], v[170:171], v[160:161]
	v_pk_add_f32 v[150:151], v[150:151], v[154:155]
	v_mov_b32_e32 v149, v185
	v_pk_fma_f32 v[172:173], v[58:59], v[58:59], v[128:129] op_sel_hi:[1,1,0]
	v_pk_fma_f32 v[168:169], v[60:61], v[60:61], v[168:169] op_sel_hi:[1,1,0]
	s_waitcnt vmcnt(17)
	v_mul_f32_e32 v183, v55, v55
	v_mul_f32_e32 v184, v54, v54
	v_pk_add_f32 v[158:159], v[158:159], v[158:159] op_sel:[0,1] op_sel_hi:[1,0]
	v_pk_add_f32 v[148:149], v[148:149], v[152:153]
	v_pk_add_f32 v[150:151], v[150:151], v[150:151] op_sel:[0,1] op_sel_hi:[1,0]
	v_pk_mul_f32 v[162:163], v[44:45], v[44:45]
	v_pk_mul_f32 v[166:167], v[42:43], v[42:43]
	v_mul_f32_e32 v173, v56, v56
	v_mul_f32_e32 v169, v57, v57
	s_waitcnt vmcnt(16)
	v_mul_f32_e32 v128, v39, v39
	v_mov_b32_e32 v159, v183
	v_pk_add_f32 v[148:149], v[148:149], v[156:157]
	v_mov_b32_e32 v151, v184
	v_pk_mov_b32 v[160:161], v[166:167], v[162:163] op_sel:[1,0]
	v_mov_b32_e32 v167, v163
	v_pk_fma_f32 v[162:163], v[38:39], v[38:39], v[128:129] op_sel_hi:[1,1,0]
	v_pk_add_f32 v[154:155], v[172:173], v[168:169]
	v_pk_add_f32 v[150:151], v[150:151], v[158:159]
	v_add_f32_e32 v128, v148, v149
	v_pk_add_f32 v[148:149], v[150:151], v[154:155]
	ds_bpermute_b32 v150, v1, v128
	v_mul_f32_e32 v174, v41, v41
	v_pk_add_f32 v[160:161], v[160:161], v[166:167]
	s_waitcnt vmcnt(15)
	v_mul_f32_e32 v181, v36, v36
	v_mul_f32_e32 v182, v37, v37
	v_mul_f32_e32 v186, v35, v35
	v_mul_f32_e32 v187, v34, v34
	v_pk_fma_f32 v[164:165], v[40:41], v[40:41], v[174:175] op_sel_hi:[1,1,0]
	v_pk_add_f32 v[160:161], v[160:161], v[160:161] op_sel:[0,1] op_sel_hi:[1,0]
	v_pk_add_f32 v[148:149], v[148:149], v[148:149] op_sel:[0,1] op_sel_hi:[1,0]
	v_mov_b32_e32 v163, v181
	v_mov_b32_e32 v165, v182
	v_mov_b32_e32 v161, v186
	v_mov_b32_e32 v149, v187
	v_pk_add_f32 v[152:153], v[162:163], v[164:165]
	v_pk_add_f32 v[148:149], v[148:149], v[160:161]
	s_waitcnt lgkmcnt(0)
	v_add_f32_e32 v128, v128, v150
	v_pk_add_f32 v[148:149], v[148:149], v[152:153]
	v_pk_add_f32 v[138:139], v[138:139], 1.0 op_sel_hi:[1,0]
	v_add_f32_e32 v148, v148, v149
	ds_bpermute_b32 v149, v129, v128
	ds_bpermute_b32 v150, v1, v148
	v_pk_add_f32 v[136:137], v[136:137], 1.0 op_sel_hi:[1,0]
	s_waitcnt lgkmcnt(1)
	v_add_f32_e32 v128, v128, v149
	s_waitcnt lgkmcnt(0)
	v_add_f32_e32 v148, v148, v150
	ds_bpermute_b32 v149, v130, v128
	ds_bpermute_b32 v150, v129, v148
	s_waitcnt lgkmcnt(1)
	v_add_f32_e32 v128, v128, v149
	s_waitcnt lgkmcnt(0)
	v_add_f32_e32 v148, v148, v150
	ds_bpermute_b32 v149, v131, v128
	ds_bpermute_b32 v150, v130, v148
	s_waitcnt lgkmcnt(1)
	v_add_f32_e32 v128, v128, v149
	s_waitcnt lgkmcnt(0)
	v_add_f32_e32 v148, v148, v150
	ds_bpermute_b32 v149, v132, v128
	ds_bpermute_b32 v150, v131, v148
	s_waitcnt lgkmcnt(1)
	v_add_f32_e32 v128, v128, v149
	s_waitcnt lgkmcnt(0)
	v_add_f32_e32 v148, v148, v150
	ds_bpermute_b32 v149, v133, v128
	ds_bpermute_b32 v150, v132, v148
	s_waitcnt lgkmcnt(1)
	v_add_f32_e32 v128, v128, v149
	s_waitcnt lgkmcnt(0)
	v_add_f32_e32 v148, v148, v150
	v_fmamk_f32 v128, v128, 0x3a000000, v134
	ds_bpermute_b32 v149, v133, v148
	v_mul_f32_e32 v150, 0x4f800000, v128
	v_cmp_gt_f32_e32 vcc, s7, v128
	s_waitcnt lgkmcnt(0)
	v_add_f32_e32 v148, v148, v149
	v_cndmask_b32_e32 v128, v128, v150, vcc
	v_sqrt_f32_e32 v150, v128
	v_fmamk_f32 v148, v148, 0x3a000000, v134
	v_mul_f32_e32 v152, 0x4f800000, v148
	v_cmp_gt_f32_e64 s[0:1], s7, v148
	v_add_u32_e32 v149, -1, v150
	v_add_u32_e32 v151, 1, v150
	v_fma_f32 v153, -v149, v150, v128
	v_fma_f32 v154, -v151, v150, v128
	v_cndmask_b32_e64 v148, v148, v152, s[0:1]
	v_cmp_ge_f32_e64 s[2:3], 0, v153
	s_nop 1
	v_cndmask_b32_e64 v149, v150, v149, s[2:3]
	v_sqrt_f32_e32 v150, v148
	v_cmp_lt_f32_e64 s[2:3], 0, v154
	s_nop 1
	v_cndmask_b32_e64 v149, v149, v151, s[2:3]
	v_mul_f32_e32 v151, 0x37800000, v149
	v_cndmask_b32_e32 v149, v149, v151, vcc
	v_cmp_class_f32_e32 vcc, v128, v135
	v_add_u32_e32 v151, 1, v150
	v_fma_f32 v155, -v151, v150, v148
	v_cndmask_b32_e32 v128, v149, v128, vcc
	v_add_u32_e32 v149, -1, v150
	v_div_scale_f32 v152, s[2:3], v128, v128, 1.0
	v_fma_f32 v154, -v149, v150, v148
	v_cmp_ge_f32_e64 s[2:3], 0, v154
	v_rcp_f32_e32 v156, v152
	v_div_scale_f32 v153, vcc, 1.0, v128, 1.0
	v_cndmask_b32_e64 v149, v150, v149, s[2:3]
	v_cmp_lt_f32_e64 s[2:3], 0, v155
	s_nop 1
	v_cndmask_b32_e64 v149, v149, v151, s[2:3]
	v_mul_f32_e32 v150, 0x37800000, v149
	v_cndmask_b32_e64 v149, v149, v150, s[0:1]
	v_cmp_class_f32_e64 s[0:1], v148, v135
	v_fma_f32 v150, -v152, v156, 1.0
	v_fmac_f32_e32 v156, v150, v156
	v_cndmask_b32_e64 v157, v149, v148, s[0:1]
	v_div_scale_f32 v158, s[0:1], v157, v157, 1.0
	v_mul_f32_e32 v148, v153, v156
	v_rcp_f32_e32 v160, v158
	v_fma_f32 v149, -v152, v148, v153
	v_fmac_f32_e32 v148, v149, v156
	v_fma_f32 v149, -v152, v148, v153
	v_div_fmas_f32 v148, v149, v156, v148
	v_fma_f32 v149, -v158, v160, 1.0
	v_div_scale_f32 v159, s[0:1], 1.0, v157, 1.0
	v_fmac_f32_e32 v160, v149, v160
	v_div_fixup_f32 v128, v148, v128, 1.0
	v_mul_f32_e32 v156, v159, v160
	v_pk_mul_f32 v[32:33], v[32:33], v[128:129] op_sel_hi:[1,0]
	v_pk_mul_f32 v[30:31], v[30:31], v[128:129] op_sel_hi:[1,0]
	v_pk_mul_f32 v[154:155], v[26:27], v[128:129] op_sel_hi:[1,0]
	v_fma_f32 v26, -v158, v156, v159
	v_pk_mul_f32 v[148:149], v[24:25], v[128:129] op_sel_hi:[1,0]
	v_pk_mul_f32 v[150:151], v[22:23], v[128:129] op_sel_hi:[1,0]
	v_pk_mul_f32 v[22:23], v[46:47], v[30:31]
	v_pk_mul_f32 v[24:25], v[48:49], v[32:33]
	v_fmac_f32_e32 v156, v26, v160
	v_pk_fma_f32 v[24:25], v[138:139], v[24:25], v[52:53]
	v_pk_fma_f32 v[22:23], v[136:137], v[22:23], v[50:51]
	v_fma_f32 v26, -v158, v156, v159
	s_mov_b64 vcc, s[0:1]
	v_cvt_pk_fp8_f32 v175, v22, v23
	v_cvt_pk_bf16_f32 v22, v22, v23
	v_cvt_pk_bf16_f32 v23, v24, v25
	v_div_fmas_f32 v26, v26, v160, v156
	global_store_dwordx2 v[120:121], v[22:23], off
	v_div_fixup_f32 v22, v26, v157, 1.0
	v_pk_mul_f32 v[152:153], v[28:29], v[128:129] op_sel_hi:[1,0]
	v_pk_mul_f32 v[26:27], v[142:143], v[22:23] op_sel_hi:[1,0]
	v_pk_mul_f32 v[28:29], v[140:141], v[22:23] op_sel_hi:[1,0]
	v_pk_mul_f32 v[26:27], v[48:49], v[26:27]
	v_pk_mul_f32 v[28:29], v[46:47], v[28:29]
	v_cvt_pk_fp8_f32 v175, v24, v25 op_sel:[0,0,1]
	v_pk_fma_f32 v[24:25], v[138:139], v[26:27], v[52:53]
	v_pk_fma_f32 v[26:27], v[136:137], v[28:29], v[50:51]
	v_pk_mul_f32 v[32:33], v[146:147], v[22:23] op_sel_hi:[1,0]
	v_cvt_pk_fp8_f32 v176, v26, v27
	v_cvt_pk_bf16_f32 v26, v26, v27
	v_cvt_pk_bf16_f32 v27, v24, v25
	global_store_dwordx2 v[126:127], v[26:27], off
	global_store_dword v[122:123], v175, off
	v_cvt_pk_fp8_f32 v176, v24, v25 op_sel:[0,0,1]
	v_pk_mul_f32 v[140:141], v[144:145], v[22:23] op_sel_hi:[1,0]
	v_pk_mul_f32 v[18:19], v[18:19], v[128:129] op_sel_hi:[1,0]
	v_pk_mul_f32 v[20:21], v[20:21], v[128:129] op_sel_hi:[1,0]
	global_store_dword v[124:125], v176, off
	s_waitcnt vmcnt(4)
; __device__ __forceinline__ unsigned pack_fp8x4(float a, float b, float c, float d) { int w = __builtin_amdgcn_cvt_pk_fp8_f32(a, b, 0, false); w = __builtin_amdgcn_cvt_pk_fp8_f32(c, d, w, true); return (unsigned)w; }
; __device__ __forceinline__ unsigned pk2(float lo, float hi) { const f32x2_t v = {lo, hi}; return __builtin_bit_cast(unsigned, __builtin_convertvector(v, bf16x2_hw)); }
; __device__ __forceinline__ void ph2_norm1(const Frame& F, const Args& A) {
;     ...
;         for (int j = 0; j < 8; ++j) { const int col = 4 * F.lane + 256 * j;
;             const f32x4 g = *(const f32x4*)(g1 + col), sh = *(const f32x4*)(MOD + col), sc = *(const f32x4*)(MOD + 2048 + col);
;             const f32x4 ha = va[j] * ra * g * (sc + 1.f) + sh, hb = vb[j] * rb * g * (sc + 1.f) + sh;
;             oa[64 * j] = (unsigned long long)pk2(ha.x, ha.y) | ((unsigned long long)pk2(ha.z, ha.w) << 32);
;             ob[64 * j] = (unsigned long long)pk2(hb.x, hb.y) | ((unsigned long long)pk2(hb.z, hb.w) << 32);
;             ((unsigned*)((unsigned char*)(A.ws + WS_XN8) + (size_t)row * DM) + F.lane)[64 * j] = pg8::pack_fp8x4(ha.x, ha.y, ha.z, ha.w);
;             ((unsigned*)((unsigned char*)(A.ws + WS_XN8) + (size_t)rowb * DM) + F.lane)[64 * j] = pg8::pack_fp8x4(hb.x, hb.y, hb.z, hb.w); }
	v_mov_b64_e32 v[24:25], v[188:189]
	v_mov_b64_e32 v[26:27], v[190:191]
	v_mov_b64_e32 v[28:29], v[192:193]
	v_mov_b64_e32 v[30:31], v[194:195]
	v_mov_b64_e32 v[46:47], v[196:197]
	v_mov_b64_e32 v[48:49], v[198:199]
	v_pk_mul_f32 v[14:15], v[14:15], v[128:129] op_sel_hi:[1,0]
	v_pk_mul_f32 v[16:17], v[16:17], v[128:129] op_sel_hi:[1,0]
	v_pk_mul_f32 v[10:11], v[10:11], v[128:129] op_sel_hi:[1,0]
	v_pk_mul_f32 v[12:13], v[12:13], v[128:129] op_sel_hi:[1,0]
	v_pk_mul_f32 v[6:7], v[6:7], v[128:129] op_sel_hi:[1,0]
	v_pk_mul_f32 v[8:9], v[8:9], v[128:129] op_sel_hi:[1,0]
	v_pk_mul_f32 v[2:3], v[2:3], v[128:129] op_sel_hi:[1,0]
	v_pk_mul_f32 v[4:5], v[4:5], v[128:129] op_sel_hi:[1,0]
	v_pk_mul_f32 v[50:51], v[150:151], v[24:25]
	v_pk_mul_f32 v[52:53], v[148:149], v[26:27]
	v_pk_mul_f32 v[26:27], v[32:33], v[26:27]
	v_pk_add_f32 v[30:31], v[30:31], 1.0 op_sel_hi:[1,0]
	v_pk_add_f32 v[28:29], v[28:29], 1.0 op_sel_hi:[1,0]
	v_pk_mul_f32 v[24:25], v[140:141], v[24:25]
	v_pk_fma_f32 v[32:33], v[52:53], v[30:31], v[48:49]
	v_pk_fma_f32 v[26:27], v[26:27], v[30:31], v[48:49]
	v_pk_fma_f32 v[30:31], v[50:51], v[28:29], v[46:47]
	v_pk_fma_f32 v[24:25], v[24:25], v[28:29], v[46:47]
	v_cvt_pk_fp8_f32 v177, v30, v31
	v_cvt_pk_fp8_f32 v178, v24, v25
	v_cvt_pk_bf16_f32 v28, v30, v31
	v_cvt_pk_bf16_f32 v29, v32, v33
	v_cvt_pk_fp8_f32 v177, v32, v33 op_sel:[0,0,1]
	v_cvt_pk_fp8_f32 v178, v26, v27 op_sel:[0,0,1]
	v_cvt_pk_bf16_f32 v24, v24, v25
	v_cvt_pk_bf16_f32 v25, v26, v27
	global_store_dwordx2 v[120:121], v[28:29], off offset:512
	global_store_dwordx2 v[126:127], v[24:25], off offset:512
	global_store_dword v[122:123], v177, off offset:256
	global_store_dword v[124:125], v178, off offset:256
	v_mov_b64_e32 v[24:25], v[200:201]
	v_mov_b64_e32 v[26:27], v[202:203]
	s_nop 0
	v_mov_b64_e32 v[28:29], v[204:205]
	v_mov_b64_e32 v[30:31], v[206:207]
	v_mov_b64_e32 v[46:47], v[208:209]
	v_mov_b64_e32 v[48:49], v[210:211]
	v_pk_mul_f32 v[32:33], v[64:65], v[22:23] op_sel_hi:[1,0]
	v_pk_mul_f32 v[50:51], v[62:63], v[22:23] op_sel_hi:[1,0]
	v_mov_b32_e32 v23, 0
	v_pk_mul_f32 v[52:53], v[154:155], v[24:25]
	v_pk_mul_f32 v[62:63], v[152:153], v[26:27]
	v_pk_mul_f32 v[26:27], v[32:33], v[26:27]
	v_pk_add_f32 v[30:31], v[30:31], 1.0 op_sel_hi:[1,0]
	v_pk_add_f32 v[28:29], v[28:29], 1.0 op_sel_hi:[1,0]
	v_pk_mul_f32 v[24:25], v[50:51], v[24:25]
	v_pk_fma_f32 v[32:33], v[62:63], v[30:31], v[48:49]
	v_pk_fma_f32 v[26:27], v[26:27], v[30:31], v[48:49]
	v_pk_fma_f32 v[30:31], v[52:53], v[28:29], v[46:47]
	v_pk_fma_f32 v[24:25], v[24:25], v[28:29], v[46:47]
	v_cvt_pk_fp8_f32 v179, v30, v31
	v_cvt_pk_fp8_f32 v180, v24, v25
	v_cvt_pk_bf16_f32 v28, v30, v31
	v_cvt_pk_bf16_f32 v29, v32, v33
	v_cvt_pk_fp8_f32 v179, v32, v33 op_sel:[0,0,1]
	v_cvt_pk_fp8_f32 v180, v26, v27 op_sel:[0,0,1]
	v_cvt_pk_bf16_f32 v24, v24, v25
	v_cvt_pk_bf16_f32 v25, v26, v27
	global_store_dwordx2 v[120:121], v[28:29], off offset:1024
	global_store_dwordx2 v[126:127], v[24:25], off offset:1024
	global_store_dword v[122:123], v179, off offset:512
	global_store_dword v[124:125], v180, off offset:512
	v_mov_b64_e32 v[24:25], v[212:213]
	v_mov_b64_e32 v[26:27], v[214:215]
	s_nop 0
	v_mov_b64_e32 v[28:29], v[216:217]
	v_mov_b64_e32 v[30:31], v[218:219]
	v_mov_b64_e32 v[46:47], v[220:221]
	v_mov_b64_e32 v[48:49], v[222:223]
	v_pk_mul_f32 v[50:51], v[58:59], v[22:23] op_sel_hi:[1,0]
	v_mov_b32_e32 v52, 0
	v_pk_mul_f32 v[32:33], v[60:61], v[22:23] op_sel_hi:[1,0]
	v_pk_mul_f32 v[18:19], v[18:19], v[24:25]
	v_pk_add_f32 v[28:29], v[28:29], 1.0 op_sel_hi:[1,0]
	v_pk_mul_f32 v[24:25], v[50:51], v[24:25]
	v_pk_fma_f32 v[18:19], v[18:19], v[28:29], v[46:47]
	v_pk_fma_f32 v[24:25], v[24:25], v[28:29], v[46:47]
	v_cvt_pk_fp8_f32 v23, v18, v19
	v_cvt_pk_fp8_f32 v52, v24, v25
	v_pk_mul_f32 v[20:21], v[20:21], v[26:27]
	v_pk_add_f32 v[30:31], v[30:31], 1.0 op_sel_hi:[1,0]
	v_pk_mul_f32 v[26:27], v[32:33], v[26:27]
	v_pk_fma_f32 v[20:21], v[20:21], v[30:31], v[48:49]
	v_pk_fma_f32 v[26:27], v[26:27], v[30:31], v[48:49]
	v_cvt_pk_fp8_f32 v23, v20, v21 op_sel:[0,0,1]
	v_cvt_pk_fp8_f32 v52, v26, v27 op_sel:[0,0,1]
	v_cvt_pk_bf16_f32 v28, v18, v19
	v_cvt_pk_bf16_f32 v29, v20, v21
	v_cvt_pk_bf16_f32 v30, v24, v25
	v_cvt_pk_bf16_f32 v31, v26, v27
	global_store_dwordx2 v[120:121], v[28:29], off offset:1536
	global_store_dwordx2 v[126:127], v[30:31], off offset:1536
	global_store_dword v[122:123], v23, off offset:768
	global_store_dword v[124:125], v52, off offset:768
	v_mov_b64_e32 v[18:19], v[224:225]
	v_mov_b64_e32 v[20:21], v[226:227]
	v_mov_b64_e32 v[24:25], v[228:229]
	v_mov_b64_e32 v[26:27], v[230:231]
	s_nop 0
	v_mov_b64_e32 v[28:29], v[232:233]
	v_mov_b64_e32 v[30:31], v[234:235]
	v_mov_b32_e32 v23, 0
	v_pk_mul_f32 v[46:47], v[54:55], v[22:23] op_sel_hi:[1,0]
	v_mov_b32_e32 v48, 0
	v_pk_mul_f32 v[32:33], v[56:57], v[22:23] op_sel_hi:[1,0]
	v_pk_mul_f32 v[14:15], v[14:15], v[18:19]
	v_pk_add_f32 v[24:25], v[24:25], 1.0 op_sel_hi:[1,0]
	v_pk_mul_f32 v[18:19], v[46:47], v[18:19]
; __device__ __forceinline__ unsigned pack_fp8x4(float a, float b, float c, float d) { int w = __builtin_amdgcn_cvt_pk_fp8_f32(a, b, 0, false); w = __builtin_amdgcn_cvt_pk_fp8_f32(c, d, w, true); return (unsigned)w; }
; __device__ __forceinline__ unsigned pk2(float lo, float hi) { const f32x2_t v = {lo, hi}; return __builtin_bit_cast(unsigned, __builtin_convertvector(v, bf16x2_hw)); }
; __device__ __forceinline__ void ph2_norm1(const Frame& F, const Args& A) {
;     ...
;         for (int j = 0; j < 8; ++j) { const int col = 4 * F.lane + 256 * j;
;             const f32x4 g = *(const f32x4*)(g1 + col), sh = *(const f32x4*)(MOD + col), sc = *(const f32x4*)(MOD + 2048 + col);
;             const f32x4 ha = va[j] * ra * g * (sc + 1.f) + sh, hb = vb[j] * rb * g * (sc + 1.f) + sh;
;             oa[64 * j] = (unsigned long long)pk2(ha.x, ha.y) | ((unsigned long long)pk2(ha.z, ha.w) << 32);
;             ob[64 * j] = (unsigned long long)pk2(hb.x, hb.y) | ((unsigned long long)pk2(hb.z, hb.w) << 32);
;             ((unsigned*)((unsigned char*)(A.ws + WS_XN8) + (size_t)row * DM) + F.lane)[64 * j] = pg8::pack_fp8x4(ha.x, ha.y, ha.z, ha.w);
;             ((unsigned*)((unsigned char*)(A.ws + WS_XN8) + (size_t)rowb * DM) + F.lane)[64 * j] = pg8::pack_fp8x4(hb.x, hb.y, hb.z, hb.w); }
	v_pk_fma_f32 v[14:15], v[14:15], v[24:25], v[28:29]
	v_pk_fma_f32 v[18:19], v[18:19], v[24:25], v[28:29]
	v_cvt_pk_fp8_f32 v23, v14, v15
	v_cvt_pk_fp8_f32 v48, v18, v19
	v_pk_mul_f32 v[16:17], v[16:17], v[20:21]
	v_pk_add_f32 v[26:27], v[26:27], 1.0 op_sel_hi:[1,0]
	v_pk_mul_f32 v[20:21], v[32:33], v[20:21]
	v_pk_fma_f32 v[16:17], v[16:17], v[26:27], v[30:31]
	v_pk_fma_f32 v[20:21], v[20:21], v[26:27], v[30:31]
	v_cvt_pk_fp8_f32 v23, v16, v17 op_sel:[0,0,1]
	v_cvt_pk_fp8_f32 v48, v20, v21 op_sel:[0,0,1]
	v_cvt_pk_bf16_f32 v24, v14, v15
	v_cvt_pk_bf16_f32 v25, v16, v17
	v_cvt_pk_bf16_f32 v26, v18, v19
	v_cvt_pk_bf16_f32 v27, v20, v21
	global_store_dwordx2 v[120:121], v[24:25], off offset:2048
	global_store_dwordx2 v[126:127], v[26:27], off offset:2048
	global_store_dword v[122:123], v23, off offset:1024
	global_store_dword v[124:125], v48, off offset:1024
	v_mov_b64_e32 v[14:15], v[236:237]
	v_mov_b64_e32 v[16:17], v[238:239]
	v_mov_b64_e32 v[18:19], v[240:241]
	v_mov_b64_e32 v[20:21], v[242:243]
	s_nop 0
	v_mov_b64_e32 v[24:25], v[244:245]
	v_mov_b64_e32 v[26:27], v[246:247]
	v_mov_b32_e32 v23, 0
	v_pk_mul_f32 v[30:31], v[42:43], v[22:23] op_sel_hi:[1,0]
	v_mov_b32_e32 v32, 0
	v_pk_mul_f32 v[28:29], v[44:45], v[22:23] op_sel_hi:[1,0]
	v_pk_mul_f32 v[10:11], v[10:11], v[14:15]
	v_pk_add_f32 v[18:19], v[18:19], 1.0 op_sel_hi:[1,0]
	v_pk_mul_f32 v[14:15], v[30:31], v[14:15]
	v_pk_fma_f32 v[10:11], v[10:11], v[18:19], v[24:25]
	v_pk_fma_f32 v[14:15], v[14:15], v[18:19], v[24:25]
	v_cvt_pk_fp8_f32 v23, v10, v11
	v_cvt_pk_fp8_f32 v32, v14, v15
	v_pk_mul_f32 v[12:13], v[12:13], v[16:17]
	v_pk_add_f32 v[20:21], v[20:21], 1.0 op_sel_hi:[1,0]
	v_pk_mul_f32 v[16:17], v[28:29], v[16:17]
	v_pk_fma_f32 v[12:13], v[12:13], v[20:21], v[26:27]
	v_pk_fma_f32 v[16:17], v[16:17], v[20:21], v[26:27]
	v_cvt_pk_fp8_f32 v23, v12, v13 op_sel:[0,0,1]
	v_cvt_pk_fp8_f32 v32, v16, v17 op_sel:[0,0,1]
	v_cvt_pk_bf16_f32 v18, v10, v11
	v_cvt_pk_bf16_f32 v19, v12, v13
	v_cvt_pk_bf16_f32 v20, v14, v15
	v_cvt_pk_bf16_f32 v21, v16, v17
	global_store_dwordx2 v[120:121], v[18:19], off offset:2560
	global_store_dwordx2 v[126:127], v[20:21], off offset:2560
	global_store_dword v[122:123], v23, off offset:1280
	global_store_dword v[124:125], v32, off offset:1280
	global_load_dwordx4 v[10:13], v[102:103], off
	global_load_dwordx4 v[14:17], v[106:107], off
	s_nop 0
	global_load_dwordx4 v[18:21], v[104:105], off
	v_mov_b32_e32 v23, 0
	v_pk_mul_f32 v[26:27], v[38:39], v[22:23] op_sel_hi:[1,0]
	v_mov_b32_e32 v28, 0
	v_pk_mul_f32 v[24:25], v[40:41], v[22:23] op_sel_hi:[1,0]
	s_waitcnt vmcnt(2)
	v_pk_mul_f32 v[6:7], v[6:7], v[10:11]
	s_waitcnt vmcnt(1)
	v_pk_add_f32 v[14:15], v[14:15], 1.0 op_sel_hi:[1,0]
	v_pk_mul_f32 v[10:11], v[26:27], v[10:11]
	s_waitcnt vmcnt(0)
	v_pk_fma_f32 v[6:7], v[6:7], v[14:15], v[18:19]
	v_pk_fma_f32 v[10:11], v[10:11], v[14:15], v[18:19]
	v_cvt_pk_fp8_f32 v23, v6, v7
	v_cvt_pk_fp8_f32 v28, v10, v11
	v_pk_mul_f32 v[8:9], v[8:9], v[12:13]
	v_pk_add_f32 v[16:17], v[16:17], 1.0 op_sel_hi:[1,0]
	v_pk_mul_f32 v[12:13], v[24:25], v[12:13]
	v_pk_fma_f32 v[8:9], v[8:9], v[16:17], v[20:21]
	v_pk_fma_f32 v[12:13], v[12:13], v[16:17], v[20:21]
	v_cvt_pk_fp8_f32 v23, v8, v9 op_sel:[0,0,1]
	v_cvt_pk_fp8_f32 v28, v12, v13 op_sel:[0,0,1]
	v_cvt_pk_bf16_f32 v14, v6, v7
	v_cvt_pk_bf16_f32 v15, v8, v9
	v_cvt_pk_bf16_f32 v16, v10, v11
	v_cvt_pk_bf16_f32 v17, v12, v13
	global_store_dwordx2 v[120:121], v[14:15], off offset:3072
	global_store_dwordx2 v[126:127], v[16:17], off offset:3072
	global_store_dword v[122:123], v23, off offset:1536
	global_store_dword v[124:125], v28, off offset:1536
	global_load_dwordx4 v[6:9], v[108:109], off
	global_load_dwordx4 v[10:13], v[112:113], off
	s_nop 0
	global_load_dwordx4 v[14:17], v[110:111], off
	v_mov_b32_e32 v23, 0
	v_pk_mul_f32 v[20:21], v[34:35], v[22:23] op_sel_hi:[1,0]
	v_mov_b32_e32 v24, 0
	v_pk_mul_f32 v[18:19], v[36:37], v[22:23] op_sel_hi:[1,0]
	s_waitcnt vmcnt(2)
	v_pk_mul_f32 v[2:3], v[2:3], v[6:7]
	s_waitcnt vmcnt(1)
	v_pk_add_f32 v[10:11], v[10:11], 1.0 op_sel_hi:[1,0]
	v_pk_mul_f32 v[6:7], v[20:21], v[6:7]
	s_waitcnt vmcnt(0)
	v_pk_fma_f32 v[2:3], v[2:3], v[10:11], v[14:15]
	v_pk_fma_f32 v[6:7], v[6:7], v[10:11], v[14:15]
	v_cvt_pk_fp8_f32 v23, v2, v3
	v_cvt_pk_fp8_f32 v24, v6, v7
	v_pk_mul_f32 v[4:5], v[4:5], v[8:9]
	v_pk_add_f32 v[12:13], v[12:13], 1.0 op_sel_hi:[1,0]
	v_pk_mul_f32 v[8:9], v[18:19], v[8:9]
	v_pk_fma_f32 v[4:5], v[4:5], v[12:13], v[16:17]
	v_pk_fma_f32 v[8:9], v[8:9], v[12:13], v[16:17]
	v_cvt_pk_fp8_f32 v23, v4, v5 op_sel:[0,0,1]
	v_cvt_pk_bf16_f32 v10, v2, v3
	v_cvt_pk_bf16_f32 v11, v4, v5
	v_cvt_pk_fp8_f32 v24, v8, v9 op_sel:[0,0,1]
	v_cvt_pk_bf16_f32 v2, v6, v7
	v_cvt_pk_bf16_f32 v3, v8, v9
	global_store_dwordx2 v[120:121], v[10:11], off offset:3584
	global_store_dwordx2 v[126:127], v[2:3], off offset:3584
	global_store_dword v[122:123], v23, off offset:1792
	global_store_dword v[124:125], v24, off offset:1792
	s_cbranch_scc1 .LBB0_167

; __device__ __forceinline__ void ph13_final(const Frame& F, const Args& A) {
;     ...
;     for (int row = gw; row < S_; row += NGW) {
;         f32x4 v[8], mo[8];
;         const f32x4* xr = (const f32x4*)(A.in[I_X] + (size_t)row * DM) + lane; const uint2* dr = (const uint2*)((const bf16*)(ws + WS_XN) + (size_t)row * DM) + lane;
; #pragma unroll
;         for (int j = 0; j < 8; ++j) { const f32x4 xv = xr[64 * j]; const uint2 dw = dr[64 * j];
;             v[j].x = xv.x + bflo(dw.x); v[j].y = xv.y + bfhi(dw.x); v[j].z = xv.z + bflo(dw.y); v[j].w = xv.w + bfhi(dw.y); mo[j] = (f32x4){0.f, 0.f, 0.f, 0.f}; }
; #pragma unroll
;         for (int k = 0; k < 4; ++k) { const int dst = EOFF[EIDX[row * 4 + k]] + ESLOT[row * 4 + k]; const unsigned* yr = (const unsigned*)(YS + (size_t)dst * DM) + lane;
; #pragma unroll
;             for (int j = 0; j < 8; ++j) { const unsigned w = yr[64 * j]; const auto lo2 = __builtin_amdgcn_cvt_pk_f32_fp8((int)w, false), hi2 = __builtin_amdgcn_cvt_pk_f32_fp8((int)w, true);
;                 mo[j].x += lo2[0]; mo[j].y += lo2[1]; mo[j].z += hi2[0]; mo[j].w += hi2[1]; } }
.LBB0_1568:
	s_ashr_i32 s7, s6, 31
	v_lshl_add_u64 v[104:105], s[8:9], 0, v[16:17]
	s_lshl_b64 s[0:1], s[6:7], 2
	v_add_co_u32_e32 v120, vcc, s3, v104
	s_add_u32 s24, s17, s0
	s_nop 0
	v_addc_co_u32_e32 v121, vcc, 0, v105, vcc
	s_addc_u32 s25, s18, s1
	global_load_dwordx2 v[42:43], v[40:41], off
	global_load_dwordx2 v[44:45], v[40:41], off offset:512
	global_load_dwordx2 v[46:47], v[40:41], off offset:1024
	global_load_dwordx2 v[48:49], v[40:41], off offset:1536
	global_load_dwordx2 v[50:51], v[40:41], off offset:2048
	global_load_dwordx2 v[52:53], v[40:41], off offset:2560
	global_load_dwordx2 v[54:55], v[40:41], off offset:3072
	global_load_dwordx2 v[56:57], v[40:41], off offset:3584
	global_load_dwordx4 v[4:7], v[20:21], off
	global_load_dwordx4 v[8:11], v[20:21], off offset:1024
	global_load_dwordx4 v[12:15], v[20:21], off offset:2048
	global_load_dwordx4 v[68:71], v[20:21], off offset:3072
	global_load_dwordx4 v[72:75], v[24:25], off
	global_load_dwordx4 v[76:79], v[26:27], off
	global_load_dwordx4 v[80:83], v[28:29], off
	global_load_dwordx4 v[84:87], v[30:31], off
	global_load_dwordx4 v[0:3], v[22:23], off
	global_load_dwordx4 v[88:91], v[104:105], off
	global_load_dwordx4 v[92:95], v[104:105], off offset:1024
	global_load_dwordx4 v[96:99], v[104:105], off offset:2048
	global_load_dwordx4 v[100:103], v[104:105], off offset:3072
	s_nop 0
	global_load_dwordx4 v[104:107], v[120:121], off
	global_load_dwordx4 v[108:111], v[120:121], off offset:1024
	global_load_dwordx4 v[112:115], v[120:121], off offset:2048
	global_load_dwordx4 v[116:119], v[120:121], off offset:3072
	s_add_u32 s0, s19, s0
	global_load_dwordx4 v[120:123], v17, s[24:25]
	s_addc_u32 s1, s20, s1
	global_load_dword v127, v17, s[0:1]
	s_add_i32 s24, s6, 1
	s_ashr_i32 s25, s24, 31
	s_lshl_b64 s[0:1], s[24:25], 2
	s_add_u32 s0, s19, s0
	s_addc_u32 s1, s20, s1
	global_load_dwordx3 v[124:126], v17, s[0:1]
	v_lshl_add_u64 v[58:59], s[12:13], 0, v[16:17]
	s_add_i32 s2, s2, s4
	s_add_i32 s6, s6, s21
	s_add_u32 s8, s8, s10
	s_addc_u32 s9, s9, s11
	s_add_u32 s12, s12, s10
	s_addc_u32 s13, s13, s11
	v_lshl_add_u64 v[40:41], v[40:41], 0, s[14:15]
	s_cmpk_lt_i32 s2, 0x2000
	s_waitcnt vmcnt(0)
	v_lshlrev_b32_e32 v128, 16, v42
	v_and_b32_e32 v129, 0xffff0000, v42
	v_lshlrev_b32_e32 v42, 16, v43
	v_and_b32_e32 v43, 0xffff0000, v43
	v_lshlrev_b32_e32 v130, 16, v44
	v_and_b32_e32 v131, 0xffff0000, v44
	v_lshlrev_b32_e32 v132, 16, v46
	v_and_b32_e32 v133, 0xffff0000, v46
	v_lshlrev_b32_e32 v136, 16, v50
	v_and_b32_e32 v137, 0xffff0000, v50
	v_lshlrev_b32_e32 v50, 16, v51
	v_and_b32_e32 v51, 0xffff0000, v51
	v_pk_add_f32 v[42:43], v[90:91], v[42:43]
	v_pk_add_f32 v[90:91], v[92:93], v[130:131]
	v_pk_add_f32 v[92:93], v[96:97], v[132:133]
	v_pk_add_f32 v[96:97], v[104:105], v[136:137]
	v_pk_add_f32 v[50:51], v[106:107], v[50:51]
	v_lshlrev_b32_e32 v104, 2, v120
	v_lshlrev_b32_e32 v105, 2, v121
	v_lshlrev_b32_e32 v107, 2, v123
	v_lshlrev_b32_e32 v46, 16, v47
	v_and_b32_e32 v47, 0xffff0000, v47
	v_lshlrev_b32_e32 v138, 16, v52
	v_and_b32_e32 v139, 0xffff0000, v52
	v_lshlrev_b32_e32 v106, 2, v122
	v_add_u32_e32 v104, s5, v104
	v_add_u32_e32 v105, s5, v105
	v_add_u32_e32 v107, s5, v107
	v_pk_add_f32 v[46:47], v[98:99], v[46:47]
	v_pk_add_f32 v[98:99], v[108:109], v[138:139]
	v_add_u32_e32 v106, s5, v106
	ds_read_b32 v104, v104
	ds_read_b32 v105, v105
	ds_read_b32 v108, v106
	ds_read_b32 v107, v107
	v_lshlrev_b32_e32 v52, 16, v53
	v_and_b32_e32 v53, 0xffff0000, v53
	s_waitcnt lgkmcnt(3)
	v_add_u32_e32 v104, v127, v104
	v_pk_add_f32 v[52:53], v[110:111], v[52:53]
	s_waitcnt lgkmcnt(2)
	v_add_u32_e32 v106, v124, v105
	s_waitcnt lgkmcnt(1)
	v_add_u32_e32 v108, v125, v108
	s_waitcnt lgkmcnt(0)
	v_add_u32_e32 v110, v126, v107
	v_ashrrev_i32_e32 v105, 31, v104
	v_ashrrev_i32_e32 v107, 31, v106
	v_ashrrev_i32_e32 v109, 31, v108
	v_ashrrev_i32_e32 v111, 31, v110
	v_lshlrev_b64 v[104:105], 11, v[104:105]
	v_lshlrev_b32_e32 v44, 16, v45
	v_and_b32_e32 v45, 0xffff0000, v45
	v_lshlrev_b32_e32 v134, 16, v48
	v_and_b32_e32 v135, 0xffff0000, v48
	v_lshlrev_b32_e32 v48, 16, v49
	v_and_b32_e32 v49, 0xffff0000, v49
	v_lshlrev_b32_e32 v140, 16, v54
	v_and_b32_e32 v141, 0xffff0000, v54
	v_lshlrev_b32_e32 v54, 16, v55
	v_and_b32_e32 v55, 0xffff0000, v55
	v_lshlrev_b32_e32 v142, 16, v56
	v_and_b32_e32 v143, 0xffff0000, v56
	v_lshlrev_b32_e32 v56, 16, v57
	v_and_b32_e32 v57, 0xffff0000, v57
	v_lshlrev_b64 v[106:107], 11, v[106:107]
	v_lshlrev_b64 v[108:109], 11, v[108:109]
	v_lshlrev_b64 v[110:111], 11, v[110:111]
	v_lshl_add_u64 v[104:105], v[18:19], 0, v[104:105]
	v_pk_add_f32 v[44:45], v[94:95], v[44:45]
	v_pk_add_f32 v[48:49], v[102:103], v[48:49]
	v_pk_add_f32 v[94:95], v[100:101], v[134:135]
	v_pk_add_f32 v[100:101], v[112:113], v[140:141]
	v_pk_add_f32 v[54:55], v[114:115], v[54:55]
	v_pk_add_f32 v[102:103], v[116:117], v[142:143]
	v_pk_add_f32 v[56:57], v[118:119], v[56:57]
	v_lshl_add_u64 v[106:107], v[18:19], 0, v[106:107]
	v_lshl_add_u64 v[108:109], v[18:19], 0, v[108:109]
	v_lshl_add_u64 v[110:111], v[18:19], 0, v[110:111]
	global_load_dword v112, v[104:105], off
	global_load_dword v113, v[104:105], off offset:256
	global_load_dword v114, v[104:105], off offset:512
	global_load_dword v118, v[104:105], off offset:768
	global_load_dword v122, v[104:105], off offset:1024
	global_load_dword v126, v[104:105], off offset:1280
	global_load_dword v130, v[104:105], off offset:1536
	global_load_dword v134, v[104:105], off offset:1792
	global_load_dword v138, v[106:107], off
	global_load_dword v142, v[106:107], off offset:256
	global_load_dword v146, v[106:107], off offset:512
	global_load_dword v150, v[106:107], off offset:768
; __device__ __forceinline__ void ph13_final(const Frame& F, const Args& A) {
;     ...
;         for (int k = 0; k < 4; ++k) { const int dst = EOFF[EIDX[row * 4 + k]] + ESLOT[row * 4 + k]; const unsigned* yr = (const unsigned*)(YS + (size_t)dst * DM) + lane;
; #pragma unroll
;             for (int j = 0; j < 8; ++j) { const unsigned w = yr[64 * j]; const auto lo2 = __builtin_amdgcn_cvt_pk_f32_fp8((int)w, false), hi2 = __builtin_amdgcn_cvt_pk_f32_fp8((int)w, true);
;                 mo[j].x += lo2[0]; mo[j].y += lo2[1]; mo[j].z += hi2[0]; mo[j].w += hi2[1]; } }
	global_load_dword v154, v[106:107], off offset:1024
	global_load_dword v158, v[106:107], off offset:1280
	global_load_dword v162, v[106:107], off offset:1536
	global_load_dword v166, v[106:107], off offset:1792
	global_load_dword v170, v[108:109], off
	global_load_dword v174, v[108:109], off offset:256
	global_load_dword v178, v[108:109], off offset:512
	global_load_dword v182, v[108:109], off offset:768
	global_load_dword v186, v[108:109], off offset:1024
	global_load_dword v190, v[108:109], off offset:1280
	global_load_dword v194, v[108:109], off offset:1536
	global_load_dword v198, v[108:109], off offset:1792
	global_load_dword v202, v[110:111], off
	global_load_dword v206, v[110:111], off offset:256
	global_load_dword v210, v[110:111], off offset:512
	global_load_dword v214, v[110:111], off offset:768
	global_load_dword v218, v[110:111], off offset:1024
	global_load_dword v222, v[110:111], off offset:1280
	global_load_dword v226, v[110:111], off offset:1536
	global_load_dword v230, v[110:111], off offset:1792
	v_pk_add_f32 v[88:89], v[88:89], v[128:129]
	v_pk_mul_f32 v[6:7], v[6:7], s[16:17] op_sel_hi:[1,0]
	v_pk_mul_f32 v[4:5], v[4:5], s[16:17] op_sel_hi:[1,0]
	v_pk_mul_f32 v[10:11], v[10:11], s[16:17] op_sel_hi:[1,0]
	v_pk_mul_f32 v[8:9], v[8:9], s[16:17] op_sel_hi:[1,0]
	v_pk_mul_f32 v[14:15], v[14:15], s[16:17] op_sel_hi:[1,0]
	v_pk_mul_f32 v[12:13], v[12:13], s[16:17] op_sel_hi:[1,0]
	v_pk_mul_f32 v[74:75], v[74:75], s[16:17] op_sel_hi:[1,0]
	v_pk_mul_f32 v[78:79], v[78:79], s[16:17] op_sel_hi:[1,0]
	v_pk_mul_f32 v[70:71], v[70:71], s[16:17] op_sel_hi:[1,0]
	v_pk_mul_f32 v[68:69], v[68:69], s[16:17] op_sel_hi:[1,0]
	v_pk_mul_f32 v[72:73], v[72:73], s[16:17] op_sel_hi:[1,0]
	v_pk_mul_f32 v[76:77], v[76:77], s[16:17] op_sel_hi:[1,0]
	v_pk_mul_f32 v[82:83], v[82:83], s[16:17] op_sel_hi:[1,0]
	v_pk_mul_f32 v[80:81], v[80:81], s[16:17] op_sel_hi:[1,0]
	v_pk_mul_f32 v[86:87], v[86:87], s[16:17] op_sel_hi:[1,0]
	v_pk_mul_f32 v[84:85], v[84:85], s[16:17] op_sel_hi:[1,0]
	s_waitcnt vmcnt(31)
	v_cvt_pk_f32_fp8_e32 v[104:105], v112
	v_cvt_pk_f32_fp8_sdwa v[106:107], v112 src0_sel:WORD_1
	s_waitcnt vmcnt(30)
	v_cvt_pk_f32_fp8_e32 v[108:109], v113
	v_cvt_pk_f32_fp8_sdwa v[110:111], v113 src0_sel:WORD_1
	s_waitcnt vmcnt(29)
	v_cvt_pk_f32_fp8_e32 v[112:113], v114
	v_cvt_pk_f32_fp8_sdwa v[114:115], v114 src0_sel:WORD_1
	s_waitcnt vmcnt(27)
	v_cvt_pk_f32_fp8_e32 v[120:121], v122
	v_cvt_pk_f32_fp8_sdwa v[122:123], v122 src0_sel:WORD_1
	s_waitcnt vmcnt(26)
	v_cvt_pk_f32_fp8_e32 v[124:125], v126
	v_cvt_pk_f32_fp8_sdwa v[126:127], v126 src0_sel:WORD_1
	s_waitcnt vmcnt(23)
	v_cvt_pk_f32_fp8_e32 v[136:137], v138
	v_cvt_pk_f32_fp8_sdwa v[138:139], v138 src0_sel:WORD_1
	s_waitcnt vmcnt(22)
	v_cvt_pk_f32_fp8_e32 v[140:141], v142
	v_cvt_pk_f32_fp8_sdwa v[142:143], v142 src0_sel:WORD_1
	v_cvt_pk_f32_fp8_e32 v[116:117], v118
	v_cvt_pk_f32_fp8_sdwa v[118:119], v118 src0_sel:WORD_1
	v_cvt_pk_f32_fp8_e32 v[128:129], v130
	v_cvt_pk_f32_fp8_sdwa v[130:131], v130 src0_sel:WORD_1
	s_waitcnt vmcnt(21)
	v_cvt_pk_f32_fp8_e32 v[144:145], v146
	v_cvt_pk_f32_fp8_sdwa v[146:147], v146 src0_sel:WORD_1
	s_waitcnt vmcnt(19)
	v_cvt_pk_f32_fp8_e32 v[152:153], v154
	v_cvt_pk_f32_fp8_sdwa v[154:155], v154 src0_sel:WORD_1
	s_waitcnt vmcnt(18)
	v_cvt_pk_f32_fp8_e32 v[156:157], v158
	v_cvt_pk_f32_fp8_sdwa v[158:159], v158 src0_sel:WORD_1
	s_waitcnt vmcnt(15)
	v_cvt_pk_f32_fp8_e32 v[168:169], v170
	v_cvt_pk_f32_fp8_sdwa v[170:171], v170 src0_sel:WORD_1
	s_waitcnt vmcnt(14)
	v_cvt_pk_f32_fp8_e32 v[172:173], v174
	v_cvt_pk_f32_fp8_sdwa v[174:175], v174 src0_sel:WORD_1
	v_cvt_pk_f32_fp8_e32 v[148:149], v150
	v_cvt_pk_f32_fp8_sdwa v[150:151], v150 src0_sel:WORD_1
	v_cvt_pk_f32_fp8_e32 v[160:161], v162
	v_cvt_pk_f32_fp8_sdwa v[162:163], v162 src0_sel:WORD_1
	s_waitcnt vmcnt(13)
	v_cvt_pk_f32_fp8_e32 v[176:177], v178
	v_cvt_pk_f32_fp8_sdwa v[178:179], v178 src0_sel:WORD_1
	s_waitcnt vmcnt(11)
	v_cvt_pk_f32_fp8_e32 v[184:185], v186
	v_cvt_pk_f32_fp8_sdwa v[186:187], v186 src0_sel:WORD_1
	s_waitcnt vmcnt(10)
	v_cvt_pk_f32_fp8_e32 v[188:189], v190
	v_cvt_pk_f32_fp8_sdwa v[190:191], v190 src0_sel:WORD_1
	s_waitcnt vmcnt(7)
	v_cvt_pk_f32_fp8_e32 v[200:201], v202
	v_cvt_pk_f32_fp8_sdwa v[202:203], v202 src0_sel:WORD_1
	s_waitcnt vmcnt(6)
	v_cvt_pk_f32_fp8_e32 v[204:205], v206
	v_cvt_pk_f32_fp8_sdwa v[206:207], v206 src0_sel:WORD_1
	v_cvt_pk_f32_fp8_e32 v[132:133], v134
	v_cvt_pk_f32_fp8_sdwa v[134:135], v134 src0_sel:WORD_1
	v_cvt_pk_f32_fp8_e32 v[180:181], v182
	v_cvt_pk_f32_fp8_sdwa v[182:183], v182 src0_sel:WORD_1
	v_cvt_pk_f32_fp8_e32 v[192:193], v194
	v_cvt_pk_f32_fp8_sdwa v[194:195], v194 src0_sel:WORD_1
	s_waitcnt vmcnt(5)
	v_cvt_pk_f32_fp8_e32 v[208:209], v210
	v_cvt_pk_f32_fp8_sdwa v[210:211], v210 src0_sel:WORD_1
	s_waitcnt vmcnt(3)
	v_cvt_pk_f32_fp8_e32 v[216:217], v218
	v_cvt_pk_f32_fp8_sdwa v[218:219], v218 src0_sel:WORD_1
	s_waitcnt vmcnt(2)
	v_cvt_pk_f32_fp8_e32 v[220:221], v222
	v_cvt_pk_f32_fp8_sdwa v[222:223], v222 src0_sel:WORD_1
	v_pk_add_f32 v[106:107], v[106:107], 0 op_sel_hi:[1,0]
	v_pk_add_f32 v[104:105], v[104:105], 0 op_sel_hi:[1,0]
	v_pk_add_f32 v[110:111], v[110:111], 0 op_sel_hi:[1,0]
	v_pk_add_f32 v[108:109], v[108:109], 0 op_sel_hi:[1,0]
	v_cvt_pk_f32_fp8_e32 v[164:165], v166
	v_cvt_pk_f32_fp8_sdwa v[166:167], v166 src0_sel:WORD_1
	v_cvt_pk_f32_fp8_e32 v[212:213], v214
	v_cvt_pk_f32_fp8_sdwa v[214:215], v214 src0_sel:WORD_1
	s_waitcnt vmcnt(1)
; __device__ __forceinline__ void ph13_final(const Frame& F, const Args& A) {
;     ...
;         for (int k = 0; k < 4; ++k) { const int dst = EOFF[EIDX[row * 4 + k]] + ESLOT[row * 4 + k]; const unsigned* yr = (const unsigned*)(YS + (size_t)dst * DM) + lane;
; #pragma unroll
;             for (int j = 0; j < 8; ++j) { const unsigned w = yr[64 * j]; const auto lo2 = __builtin_amdgcn_cvt_pk_f32_fp8((int)w, false), hi2 = __builtin_amdgcn_cvt_pk_f32_fp8((int)w, true);
;                 mo[j].x += lo2[0]; mo[j].y += lo2[1]; mo[j].z += hi2[0]; mo[j].w += hi2[1]; } }
;         float ss = 0.f;
; #pragma unroll
;         for (int j = 0; j < 8; ++j) { const f32x4 g2 = *(const f32x4*)(MOD + 10240 + 4 * lane + 256 * j) * 0.03125f; v[j] = v[j] + g2 * mo[j];
;             ss += (v[j].x * v[j].x + v[j].y * v[j].y) + (v[j].z * v[j].z + v[j].w * v[j].w); }
;         const float rstd = 1.f / sqrtf(wave_sum(ss) * (1.f / DM) + EPS_);
	v_cvt_pk_f32_fp8_e32 v[224:225], v226
	v_cvt_pk_f32_fp8_sdwa v[226:227], v226 src0_sel:WORD_1
	v_pk_add_f32 v[112:113], v[112:113], 0 op_sel_hi:[1,0]
	v_pk_add_f32 v[114:115], v[114:115], 0 op_sel_hi:[1,0]
	v_pk_add_f32 v[122:123], v[122:123], 0 op_sel_hi:[1,0]
	v_pk_add_f32 v[126:127], v[126:127], 0 op_sel_hi:[1,0]
	v_pk_add_f32 v[104:105], v[104:105], v[136:137]
	v_pk_add_f32 v[106:107], v[106:107], v[138:139]
	v_pk_add_f32 v[108:109], v[108:109], v[140:141]
	v_pk_add_f32 v[110:111], v[110:111], v[142:143]
	v_cvt_pk_f32_fp8_e32 v[196:197], v198
	v_cvt_pk_f32_fp8_sdwa v[198:199], v198 src0_sel:WORD_1
	v_pk_add_f32 v[118:119], v[118:119], 0 op_sel_hi:[1,0]
	v_pk_add_f32 v[116:117], v[116:117], 0 op_sel_hi:[1,0]
	v_pk_add_f32 v[120:121], v[120:121], 0 op_sel_hi:[1,0]
	v_pk_add_f32 v[124:125], v[124:125], 0 op_sel_hi:[1,0]
	v_pk_add_f32 v[130:131], v[130:131], 0 op_sel_hi:[1,0]
	v_pk_add_f32 v[128:129], v[128:129], 0 op_sel_hi:[1,0]
	v_pk_add_f32 v[114:115], v[114:115], v[146:147]
	v_pk_add_f32 v[112:113], v[112:113], v[144:145]
	v_pk_add_f32 v[122:123], v[122:123], v[154:155]
	v_pk_add_f32 v[126:127], v[126:127], v[158:159]
	v_pk_add_f32 v[106:107], v[106:107], v[170:171]
	v_pk_add_f32 v[104:105], v[104:105], v[168:169]
	v_pk_add_f32 v[110:111], v[110:111], v[174:175]
	v_pk_add_f32 v[108:109], v[108:109], v[172:173]
	s_waitcnt vmcnt(0)
	v_cvt_pk_f32_fp8_e32 v[228:229], v230
	v_cvt_pk_f32_fp8_sdwa v[230:231], v230 src0_sel:WORD_1
	v_pk_add_f32 v[116:117], v[116:117], v[148:149]
	v_pk_add_f32 v[118:119], v[118:119], v[150:151]
	v_pk_add_f32 v[120:121], v[120:121], v[152:153]
	v_pk_add_f32 v[124:125], v[124:125], v[156:157]
	v_pk_add_f32 v[128:129], v[128:129], v[160:161]
	v_pk_add_f32 v[130:131], v[130:131], v[162:163]
	v_pk_add_f32 v[112:113], v[112:113], v[176:177]
	v_pk_add_f32 v[114:115], v[114:115], v[178:179]
	v_pk_add_f32 v[122:123], v[122:123], v[186:187]
	v_pk_add_f32 v[126:127], v[126:127], v[190:191]
	v_pk_add_f32 v[104:105], v[104:105], v[200:201]
	v_pk_add_f32 v[106:107], v[106:107], v[202:203]
	v_pk_add_f32 v[108:109], v[108:109], v[204:205]
	v_pk_add_f32 v[110:111], v[110:111], v[206:207]
	v_pk_add_f32 v[134:135], v[134:135], 0 op_sel_hi:[1,0]
	v_pk_add_f32 v[132:133], v[132:133], 0 op_sel_hi:[1,0]
	v_pk_add_f32 v[118:119], v[118:119], v[182:183]
	v_pk_add_f32 v[116:117], v[116:117], v[180:181]
	v_pk_add_f32 v[120:121], v[120:121], v[184:185]
	v_pk_add_f32 v[124:125], v[124:125], v[188:189]
	v_pk_add_f32 v[130:131], v[130:131], v[194:195]
	v_pk_add_f32 v[128:129], v[128:129], v[192:193]
	v_pk_add_f32 v[114:115], v[114:115], v[210:211]
	v_pk_add_f32 v[112:113], v[112:113], v[208:209]
	v_pk_add_f32 v[122:123], v[122:123], v[218:219]
	v_pk_add_f32 v[126:127], v[126:127], v[222:223]
	v_pk_fma_f32 v[6:7], v[106:107], v[6:7], v[42:43]
	v_pk_fma_f32 v[4:5], v[104:105], v[4:5], v[88:89]
	v_pk_fma_f32 v[10:11], v[110:111], v[10:11], v[44:45]
	v_pk_fma_f32 v[8:9], v[108:109], v[8:9], v[90:91]
	v_pk_add_f32 v[132:133], v[132:133], v[164:165]
	v_pk_add_f32 v[134:135], v[134:135], v[166:167]
	v_pk_add_f32 v[116:117], v[116:117], v[212:213]
	v_pk_add_f32 v[118:119], v[118:119], v[214:215]
	v_pk_add_f32 v[120:121], v[120:121], v[216:217]
	v_pk_add_f32 v[124:125], v[124:125], v[220:221]
	v_pk_add_f32 v[128:129], v[128:129], v[224:225]
	v_pk_add_f32 v[130:131], v[130:131], v[226:227]
	v_pk_fma_f32 v[12:13], v[112:113], v[12:13], v[92:93]
	v_pk_fma_f32 v[14:15], v[114:115], v[14:15], v[46:47]
	v_pk_fma_f32 v[46:47], v[122:123], v[74:75], v[50:51]
	v_pk_fma_f32 v[52:53], v[126:127], v[78:79], v[52:53]
	v_mov_b32_e32 v74, v5
	v_mov_b32_e32 v75, v9
	v_mov_b32_e32 v78, v7
	v_mov_b32_e32 v79, v11
	v_pk_add_f32 v[134:135], v[134:135], v[198:199]
	v_pk_add_f32 v[132:133], v[132:133], v[196:197]
	v_pk_fma_f32 v[42:43], v[118:119], v[70:71], v[48:49]
	v_pk_fma_f32 v[44:45], v[116:117], v[68:69], v[94:95]
	v_pk_fma_f32 v[48:49], v[120:121], v[72:73], v[96:97]
	v_pk_fma_f32 v[50:51], v[124:125], v[76:77], v[98:99]
	v_pk_fma_f32 v[54:55], v[130:131], v[82:83], v[54:55]
	v_pk_fma_f32 v[68:69], v[128:129], v[80:81], v[100:101]
	v_mov_b32_e32 v72, v4
	v_mov_b32_e32 v73, v8
	v_mov_b32_e32 v76, v6
	v_mov_b32_e32 v77, v10
	v_pk_mul_f32 v[80:81], v[14:15], v[14:15]
	v_pk_mul_f32 v[82:83], v[12:13], v[12:13]
	v_pk_mul_f32 v[74:75], v[74:75], v[74:75]
	v_pk_mul_f32 v[78:79], v[78:79], v[78:79]
	v_pk_add_f32 v[132:133], v[132:133], v[228:229]
	v_pk_add_f32 v[134:135], v[134:135], v[230:231]
	v_pk_mov_b32 v[96:97], v[82:83], v[80:81] op_sel:[1,0]
	v_mov_b32_e32 v83, v81
	v_pk_fma_f32 v[72:73], v[72:73], v[72:73], v[74:75]
	v_pk_fma_f32 v[74:75], v[76:77], v[76:77], v[78:79]
	v_pk_fma_f32 v[56:57], v[134:135], v[86:87], v[56:57]
	v_pk_fma_f32 v[70:71], v[132:133], v[84:85], v[102:103]
	v_mul_f32_e32 v84, v45, v45
	v_mul_f32_e32 v86, v43, v43
	v_pk_add_f32 v[76:77], v[96:97], v[82:83]
	v_pk_add_f32 v[72:73], v[72:73], v[74:75]
	v_mul_f32_e32 v95, v48, v48
	v_mul_f32_e32 v98, v49, v49
	v_mul_f32_e32 v99, v46, v46
	v_mul_f32_e32 v100, v47, v47
	v_pk_fma_f32 v[80:81], v[44:45], v[44:45], v[84:85] op_sel_hi:[1,1,0]
	v_pk_fma_f32 v[84:85], v[42:43], v[42:43], v[86:87] op_sel_hi:[1,1,0]
	v_pk_add_f32 v[74:75], v[76:77], v[76:77] op_sel:[0,1] op_sel_hi:[1,0]
	v_pk_add_f32 v[72:73], v[72:73], v[72:73] op_sel:[0,1] op_sel_hi:[1,0]
	v_pk_mul_f32 v[88:89], v[52:53], v[52:53]
	v_pk_mul_f32 v[90:91], v[50:51], v[50:51]
	v_mov_b32_e32 v81, v99
	v_mov_b32_e32 v85, v100
	v_mov_b32_e32 v75, v98
	v_mov_b32_e32 v73, v95
	v_pk_mov_b32 v[86:87], v[90:91], v[88:89] op_sel:[1,0]
	v_mov_b32_e32 v91, v89
	v_pk_add_f32 v[76:77], v[80:81], v[84:85]
	v_pk_add_f32 v[72:73], v[72:73], v[74:75]
	v_mul_f32_e32 v92, v69, v69
	v_mul_f32_e32 v94, v55, v55
	v_pk_add_f32 v[78:79], v[86:87], v[90:91]
	v_pk_add_f32 v[72:73], v[72:73], v[76:77]
	v_mul_f32_e32 v101, v70, v70
	v_mul_f32_e32 v102, v71, v71
	v_mul_f32_e32 v103, v56, v56
	v_mul_f32_e32 v104, v57, v57
	v_pk_fma_f32 v[88:89], v[68:69], v[68:69], v[92:93] op_sel_hi:[1,1,0]
	v_pk_fma_f32 v[92:93], v[54:55], v[54:55], v[94:95] op_sel_hi:[1,1,0]
	v_pk_add_f32 v[78:79], v[78:79], v[78:79] op_sel:[0,1] op_sel_hi:[1,0]
	v_pk_add_f32 v[72:73], v[72:73], v[72:73] op_sel:[0,1] op_sel_hi:[1,0]
	v_mov_b32_e32 v89, v103
	v_mov_b32_e32 v93, v104
	v_mov_b32_e32 v79, v102
	v_mov_b32_e32 v73, v101
	v_pk_add_f32 v[80:81], v[88:89], v[92:93]
	v_pk_add_f32 v[72:73], v[72:73], v[78:79]
	s_nop 0
	v_pk_add_f32 v[72:73], v[72:73], v[80:81]
	s_nop 0
	v_add_f32_e32 v72, v72, v73
	global_load_dwordx4 v[204:207], v[22:23], off offset:1024
	global_load_dwordx4 v[208:211], v[22:23], off offset:2048
	global_load_dwordx4 v[212:215], v[22:23], off offset:3072
	global_load_dwordx4 v[216:219], v[32:33], off
	global_load_dwordx4 v[220:223], v[34:35], off
	global_load_dwordx4 v[224:227], v[36:37], off
	global_load_dwordx4 v[228:231], v[38:39], off
	ds_bpermute_b32 v73, v60, v72
	s_waitcnt lgkmcnt(0)
; __device__ __forceinline__ void ph13_final(const Frame& F, const Args& A) {
;     ...
;         for (int j = 0; j < 8; ++j) { const f32x4 g2 = *(const f32x4*)(MOD + 10240 + 4 * lane + 256 * j) * 0.03125f; v[j] = v[j] + g2 * mo[j];
;             ss += (v[j].x * v[j].x + v[j].y * v[j].y) + (v[j].z * v[j].z + v[j].w * v[j].w); }
;         const float rstd = 1.f / sqrtf(wave_sum(ss) * (1.f / DM) + EPS_);
;         f32x4* orow = (f32x4*)(out + (size_t)row * DM) + lane;
; #pragma unroll
;         for (int j = 0; j < 8; ++j) { const f32x4 g = *(const f32x4*)(fg + 4 * lane + 256 * j); orow[64 * j] = v[j] * rstd * g; }
	v_add_f32_e32 v72, v72, v73
	ds_bpermute_b32 v73, v61, v72
	s_waitcnt lgkmcnt(0)
	v_add_f32_e32 v72, v72, v73
	ds_bpermute_b32 v73, v62, v72
	s_waitcnt lgkmcnt(0)
	v_add_f32_e32 v72, v72, v73
	ds_bpermute_b32 v73, v63, v72
	s_waitcnt lgkmcnt(0)
	v_add_f32_e32 v72, v72, v73
	ds_bpermute_b32 v73, v64, v72
	s_waitcnt lgkmcnt(0)
	v_add_f32_e32 v72, v72, v73
	ds_bpermute_b32 v73, v65, v72
	s_waitcnt lgkmcnt(0)
	v_add_f32_e32 v72, v72, v73
	v_fmamk_f32 v72, v72, 0x3a000000, v66
	v_mul_f32_e32 v73, 0x4f800000, v72
	v_cmp_gt_f32_e32 vcc, s22, v72
	s_nop 1
	v_cndmask_b32_e32 v72, v72, v73, vcc
	v_sqrt_f32_e32 v73, v72
	s_nop 0
	v_add_u32_e32 v74, -1, v73
	v_add_u32_e32 v75, 1, v73
	v_fma_f32 v76, -v74, v73, v72
	v_fma_f32 v77, -v75, v73, v72
	v_cmp_ge_f32_e64 s[0:1], 0, v76
	s_nop 1
	v_cndmask_b32_e64 v73, v73, v74, s[0:1]
	v_cmp_lt_f32_e64 s[0:1], 0, v77
	s_nop 1
	v_cndmask_b32_e64 v73, v73, v75, s[0:1]
	v_mul_f32_e32 v74, 0x37800000, v73
	v_cndmask_b32_e32 v73, v73, v74, vcc
	v_cmp_class_f32_e32 vcc, v72, v67
	s_nop 1
	v_cndmask_b32_e32 v72, v73, v72, vcc
	v_div_scale_f32 v73, s[0:1], v72, v72, 1.0
	v_rcp_f32_e32 v75, v73
	v_div_scale_f32 v74, vcc, 1.0, v72, 1.0
	v_fma_f32 v76, -v73, v75, 1.0
	v_fmac_f32_e32 v75, v76, v75
	v_mul_f32_e32 v76, v74, v75
	v_fma_f32 v77, -v73, v76, v74
	v_fmac_f32_e32 v76, v77, v75
	v_fma_f32 v73, -v73, v76, v74
	v_div_fmas_f32 v73, v73, v75, v76
	v_div_fixup_f32 v72, v73, v72, 1.0
	v_pk_mul_f32 v[4:5], v[4:5], v[72:73] op_sel_hi:[1,0]
	v_pk_mul_f32 v[6:7], v[6:7], v[72:73] op_sel_hi:[1,0]
	v_pk_mul_f32 v[0:1], v[0:1], v[4:5]
	v_pk_mul_f32 v[2:3], v[2:3], v[6:7]
	global_store_dwordx4 v[58:59], v[0:3], off
	s_waitcnt vmcnt(1)
	s_nop 0
	v_mov_b64_e32 v[0:1], v[204:205]
	v_mov_b64_e32 v[2:3], v[206:207]
	v_pk_mul_f32 v[4:5], v[10:11], v[72:73] op_sel_hi:[1,0]
	v_pk_mul_f32 v[6:7], v[8:9], v[72:73] op_sel_hi:[1,0]
	v_pk_mul_f32 v[8:9], v[48:49], v[72:73] op_sel_hi:[1,0]
	v_pk_mul_f32 v[0:1], v[0:1], v[6:7]
	v_pk_mul_f32 v[2:3], v[2:3], v[4:5]
	global_store_dwordx4 v[58:59], v[0:3], off offset:1024
	s_nop 1
	v_mov_b64_e32 v[0:1], v[208:209]
	v_mov_b64_e32 v[2:3], v[210:211]
	v_pk_mul_f32 v[4:5], v[14:15], v[72:73] op_sel_hi:[1,0]
	v_pk_mul_f32 v[6:7], v[12:13], v[72:73] op_sel_hi:[1,0]
	v_pk_mul_f32 v[2:3], v[2:3], v[4:5]
	v_pk_mul_f32 v[0:1], v[0:1], v[6:7]
	global_store_dwordx4 v[58:59], v[0:3], off offset:2048
	s_nop 1
	v_mov_b64_e32 v[0:1], v[212:213]
	v_mov_b64_e32 v[2:3], v[214:215]
	v_pk_mul_f32 v[4:5], v[42:43], v[72:73] op_sel_hi:[1,0]
	v_pk_mul_f32 v[6:7], v[44:45], v[72:73] op_sel_hi:[1,0]
	v_pk_mul_f32 v[2:3], v[2:3], v[4:5]
	v_pk_mul_f32 v[0:1], v[0:1], v[6:7]
	global_store_dwordx4 v[58:59], v[0:3], off offset:3072
	s_nop 1
	v_mov_b64_e32 v[0:1], v[216:217]
	v_mov_b64_e32 v[2:3], v[218:219]
	v_add_co_u32_e32 v4, vcc, s3, v58
	v_pk_mul_f32 v[6:7], v[46:47], v[72:73] op_sel_hi:[1,0]
	s_nop 0
	v_addc_co_u32_e32 v5, vcc, 0, v59, vcc
	v_pk_mul_f32 v[0:1], v[0:1], v[8:9]
	v_pk_mul_f32 v[2:3], v[2:3], v[6:7]
	global_store_dwordx4 v[4:5], v[0:3], off
	s_nop 1
	v_mov_b64_e32 v[0:1], v[220:221]
	v_mov_b64_e32 v[2:3], v[222:223]
	v_pk_mul_f32 v[6:7], v[52:53], v[72:73] op_sel_hi:[1,0]
	v_pk_mul_f32 v[8:9], v[50:51], v[72:73] op_sel_hi:[1,0]
	v_pk_mul_f32 v[2:3], v[2:3], v[6:7]
	v_pk_mul_f32 v[0:1], v[0:1], v[8:9]
	global_store_dwordx4 v[4:5], v[0:3], off offset:1024
	s_nop 1
	v_mov_b64_e32 v[0:1], v[224:225]
	v_mov_b64_e32 v[2:3], v[226:227]
	v_pk_mul_f32 v[6:7], v[54:55], v[72:73] op_sel_hi:[1,0]
	v_pk_mul_f32 v[8:9], v[68:69], v[72:73] op_sel_hi:[1,0]
	v_pk_mul_f32 v[2:3], v[2:3], v[6:7]
	v_pk_mul_f32 v[0:1], v[0:1], v[8:9]
	global_store_dwordx4 v[4:5], v[0:3], off offset:2048
	s_nop 1
	v_mov_b64_e32 v[0:1], v[228:229]
	v_mov_b64_e32 v[2:3], v[230:231]
	v_pk_mul_f32 v[6:7], v[56:57], v[72:73] op_sel_hi:[1,0]
	v_pk_mul_f32 v[8:9], v[70:71], v[72:73] op_sel_hi:[1,0]
	v_pk_mul_f32 v[2:3], v[6:7], v[2:3]
	v_pk_mul_f32 v[0:1], v[8:9], v[0:1]
	global_store_dwordx4 v[4:5], v[0:3], off offset:3072
	s_cbranch_scc1 .LBB0_1568
